# speedup vs baseline: 1.0681x; 1.0681x over previous
_Z14seg_sum_kernelPKfS0_S0_PDv8_DF16bS2_Pf:
	s_ashr_i32 s4, s2, 2
	s_load_dwordx4 s[12:15], s[0:1], 0x0
	s_and_b32 s3, s2, 7
	s_and_b32 s4, s4, -8
	s_or_b32 s3, s4, s3
	v_readfirstlane_b32 s5, v0
	s_ashr_i32 s4, s3, 2
	s_lshr_b32 s11, s5, 6
	s_mul_hi_u32 s5, s5, 0xaaaaaaab
	s_lshr_b32 s23, s5, 7
	s_ashr_i32 s5, s4, 31
	s_and_b32 s22, s2, 3
	s_lshl_b64 s[6:7], s[4:5], 19
	s_waitcnt lgkmcnt(0)
	s_add_u32 s5, s14, s6
	s_addc_u32 s6, s15, s7
	s_lshl_b32 s14, s22, 10
	s_lshl_b32 s8, s22, 12
	s_add_u32 s8, s5, s8
	v_lshlrev_b32_e32 v2, 6, v0
	v_add_u32_e32 v122, 0x300, v0
	s_addc_u32 s9, s6, 0
	v_lshlrev_b32_e32 v1, 4, v0
	v_and_b32_e32 v2, 0xc000, v2
	v_mov_b32_e32 v3, 0
	v_lshlrev_b32_e32 v6, 6, v122
	v_lshl_add_u64 v[4:5], s[8:9], 0, v[2:3]
	v_and_b32_e32 v2, 0xff0, v1
	v_lshlrev_b32_e32 v1, 4, v122
	v_and_b32_e32 v6, 0x1c000, v6
	v_mov_b32_e32 v7, v3
	v_lshl_add_u64 v[4:5], v[4:5], 0, v[2:3]
	v_lshl_add_u64 v[6:7], s[8:9], 0, v[6:7]
	v_and_b32_e32 v8, 0xff0, v1
	v_mov_b32_e32 v9, v3
	v_add_u32_e32 v123, 0x600, v0
	v_lshl_add_u64 v[6:7], v[6:7], 0, v[8:9]
	global_load_dwordx4 v[82:85], v[4:5], off nt
	global_load_dwordx4 v[78:81], v[6:7], off nt
	v_lshlrev_b32_e32 v4, 6, v123
	v_lshlrev_b32_e32 v1, 4, v123
	v_and_b32_e32 v4, 0x3c000, v4
	v_mov_b32_e32 v5, v3
	v_lshl_add_u64 v[4:5], s[8:9], 0, v[4:5]
	v_and_b32_e32 v6, 0xff0, v1
	v_mov_b32_e32 v7, v3
	v_add_u32_e32 v124, 0x900, v0
	v_lshl_add_u64 v[4:5], v[4:5], 0, v[6:7]
	v_lshlrev_b32_e32 v6, 6, v124
	v_lshlrev_b32_e32 v1, 4, v124
	v_and_b32_e32 v6, 0x3c000, v6
	v_lshl_add_u64 v[6:7], s[8:9], 0, v[6:7]
	v_and_b32_e32 v8, 0xff0, v1
	v_or_b32_e32 v125, 0xc00, v0
	v_lshl_add_u64 v[6:7], v[6:7], 0, v[8:9]
	v_lshlrev_b32_e32 v1, 6, v125
	v_add_u32_e32 v130, 0xf00, v0
	global_load_dwordx4 v[90:93], v[4:5], off nt
	global_load_dwordx4 v[86:89], v[6:7], off nt
	v_and_b32_e32 v4, 0x3c000, v1
	v_mov_b32_e32 v5, v3
	v_lshlrev_b32_e32 v6, 6, v130
	v_lshl_add_u64 v[4:5], s[8:9], 0, v[4:5]
	v_lshlrev_b32_e32 v1, 4, v130
	v_and_b32_e32 v6, 0x7c000, v6
	v_mov_b32_e32 v7, v3
	v_lshl_add_u64 v[4:5], v[4:5], 0, v[2:3]
	v_lshl_add_u64 v[6:7], s[8:9], 0, v[6:7]
	v_and_b32_e32 v8, 0xff0, v1
	v_add_u32_e32 v131, 0x1200, v0
	v_lshl_add_u64 v[6:7], v[6:7], 0, v[8:9]
	global_load_dwordx4 v[98:101], v[4:5], off nt
	global_load_dwordx4 v[94:97], v[6:7], off nt
	v_lshlrev_b32_e32 v4, 6, v131
	v_lshlrev_b32_e32 v1, 4, v131
	v_and_b32_e32 v4, 0x5c000, v4
	v_mov_b32_e32 v5, v3
	v_lshl_add_u64 v[4:5], s[8:9], 0, v[4:5]
	v_and_b32_e32 v6, 0xff0, v1
	v_mov_b32_e32 v7, v3
	v_add_u32_e32 v134, 0x1500, v0
	v_lshl_add_u64 v[4:5], v[4:5], 0, v[6:7]
	v_lshlrev_b32_e32 v6, 6, v134
	v_lshlrev_b32_e32 v1, 4, v134
	v_and_b32_e32 v6, 0x7c000, v6
	v_or_b32_e32 v135, 0x1800, v0
	v_lshl_add_u64 v[6:7], s[8:9], 0, v[6:7]
	v_and_b32_e32 v8, 0xff0, v1
	v_lshlrev_b32_e32 v1, 6, v135
	v_lshl_add_u64 v[6:7], v[6:7], 0, v[8:9]
	global_load_dwordx4 v[106:109], v[4:5], off nt
	global_load_dwordx4 v[102:105], v[6:7], off nt
	v_and_b32_e32 v4, 0x6c000, v1
	v_mov_b32_e32 v5, v3
	v_lshl_add_u64 v[4:5], s[8:9], 0, v[4:5]
	v_add_u32_e32 v136, 0x1b00, v0
	v_lshl_add_u64 v[4:5], v[4:5], 0, v[2:3]
	v_lshlrev_b32_e32 v2, 6, v136
	v_lshlrev_b32_e32 v1, 4, v136
	v_and_b32_e32 v2, 0x7c000, v2
	v_lshl_add_u64 v[6:7], s[8:9], 0, v[2:3]
	v_and_b32_e32 v2, 0xff0, v1
	v_add_u32_e32 v137, 0x1e00, v0
	v_lshl_add_u64 v[6:7], v[6:7], 0, v[2:3]
	v_min_u32_e32 v1, 0x1fff, v137
	global_load_dwordx4 v[118:121], v[4:5], off nt
	global_load_dwordx4 v[110:113], v[6:7], off nt
	v_lshlrev_b32_e32 v6, 4, v1
	v_lshlrev_b32_e32 v1, 6, v1
	v_and_b32_e32 v2, 0x7c000, v1
	v_bfe_u32 v127, v0, 4, 2
	s_lshl_b32 s4, s4, 12
	v_lshl_add_u64 v[4:5], s[8:9], 0, v[2:3]
	v_and_b32_e32 v2, 0xff0, v6
	v_lshlrev_b32_e32 v133, 3, v127
	s_or_b32 s4, s14, s4
	v_lshl_add_u64 v[4:5], v[4:5], 0, v[2:3]
	s_lshl_b32 s26, s23, 8
	v_or_b32_e32 v2, s4, v133
	s_movk_i32 s10, 0xc00
	global_load_dwordx4 v[114:117], v[4:5], off nt
	s_mul_hi_u32 s6, s11, 0x55555556
	v_add_u32_e32 v28, s26, v2
	v_mov_b64_e32 v[4:5], s[12:13]
	s_mov_b32 s7, 0
	s_bfe_u32 s24, s2, 0x20003
	s_mul_i32 s6, s6, 3
	v_mad_i64_i32 v[4:5], s[8:9], v28, s10, v[4:5]
	s_sub_i32 s25, s11, s6
	s_mul_i32 s8, s24, 0x300
	s_mov_b32 s9, s7
	v_and_b32_e32 v1, 15, v0
	v_lshl_add_u64 v[4:5], v[4:5], 0, s[8:9]
	s_lshl_b32 s8, s25, 8
	v_lshl_add_u64 v[4:5], v[4:5], 0, s[8:9]
	v_lshlrev_b32_e32 v2, 4, v1
	v_lshl_add_u64 v[4:5], v[4:5], 0, v[2:3]
	s_movk_i32 s4, 0x1000
	v_add_co_u32_e32 v6, vcc, s4, v4
	s_movk_i32 s4, 0x2000
	s_nop 0
	v_addc_co_u32_e32 v7, vcc, 0, v5, vcc
	v_add_co_u32_e32 v8, vcc, s4, v4
	s_movk_i32 s4, 0x3000
	s_nop 0
	v_addc_co_u32_e32 v9, vcc, 0, v5, vcc
	global_load_dwordx4 v[18:21], v[4:5], off nt
	global_load_dwordx4 v[30:33], v[4:5], off offset:3072 nt
	global_load_dwordx4 v[46:49], v[6:7], off offset:2048 nt
	global_load_dwordx4 v[50:53], v[8:9], off offset:1024 nt
	v_add_co_u32_e32 v6, vcc, s4, v4
	s_movk_i32 s4, 0x4000
	s_nop 0
	v_addc_co_u32_e32 v7, vcc, 0, v5, vcc
	global_load_dwordx4 v[62:65], v[6:7], off nt
	global_load_dwordx4 v[66:69], v[6:7], off offset:3072 nt
	v_add_co_u32_e32 v6, vcc, s4, v4
	s_movk_i32 s4, 0x5000
	s_nop 0
	v_addc_co_u32_e32 v7, vcc, 0, v5, vcc
	v_add_co_u32_e32 v8, vcc, s4, v4
	s_mov_b32 s4, 0x18000
	s_nop 0
	v_addc_co_u32_e32 v9, vcc, 0, v5, vcc
	v_add_co_u32_e32 v10, vcc, s4, v4
	s_mov_b32 s4, 0x19000
	s_nop 0
	v_addc_co_u32_e32 v11, vcc, 0, v5, vcc
	v_add_co_u32_e32 v14, vcc, s4, v4
	s_mov_b32 s4, 0x1a000
	s_nop 0
	v_addc_co_u32_e32 v15, vcc, 0, v5, vcc
	v_add_co_u32_e32 v22, vcc, s4, v4
	s_mov_b32 s4, 0x1b000
	s_nop 0
	v_addc_co_u32_e32 v23, vcc, 0, v5, vcc
	v_add_co_u32_e32 v26, vcc, s4, v4
	s_mov_b32 s5, 0x1c000
	s_nop 0
	v_addc_co_u32_e32 v27, vcc, 0, v5, vcc
	global_load_dwordx4 v[70:73], v[6:7], off offset:2048 nt
	global_load_dwordx4 v[74:77], v[8:9], off offset:1024 nt
	s_nop 0
	global_load_dwordx4 v[6:9], v[10:11], off nt
	s_nop 0
	global_load_dwordx4 v[10:13], v[10:11], off offset:3072 nt
	s_nop 0
	global_load_dwordx4 v[14:17], v[14:15], off offset:2048 nt
	s_nop 0
	global_load_dwordx4 v[22:25], v[22:23], off offset:1024 nt
	s_nop 0
	global_load_dwordx4 v[38:41], v[26:27], off nt
	global_load_dwordx4 v[42:45], v[26:27], off offset:3072 nt
	v_add_co_u32_e32 v26, vcc, s5, v4
	s_mov_b32 s4, 0x1d000
	s_nop 0
	v_addc_co_u32_e32 v27, vcc, 0, v5, vcc
	v_add_co_u32_e32 v4, vcc, s4, v4
	v_lshrrev_b32_e32 v126, 3, v0
	s_nop 0
	v_addc_co_u32_e32 v5, vcc, 0, v5, vcc
	global_load_dwordx4 v[54:57], v[26:27], off offset:2048 nt
	global_load_dwordx4 v[58:61], v[4:5], off offset:1024 nt
	v_mad_i64_i32 v[4:5], s[4:5], v28, s10, 0
	s_lshl_b32 s4, s2, 1
	s_nop 0
	v_bfi_b32 v132, -8, s4, v0
	v_mad_u64_u32 v[128:129], s[4:5], s22, 24, v[126:127]
	s_movk_i32 s4, 0xc0
	s_lshl_b32 s6, s25, 6
	v_cmp_gt_u32_e64 s[4:5], s4, v0
	v_mov_b32_e32 v26, v3
	v_mov_b32_e32 v27, v3
	v_mov_b32_e32 v28, v3
	v_mov_b32_e32 v29, v3
	v_mov_b32_e32 v34, v3
	v_mov_b32_e32 v35, v3
	v_mov_b32_e32 v36, v3
	v_mov_b32_e32 v37, v3
	s_and_saveexec_b64 s[8:9], s[4:5]
	s_cbranch_execz .LBB0_2
	s_load_dwordx2 s[14:15], s[0:1], 0x10
	v_lshlrev_b32_e32 v26, 5, v128
	v_mov_b32_e32 v27, 0
	s_waitcnt lgkmcnt(0)
	v_mov_b64_e32 v[28:29], s[14:15]
	v_mad_i64_i32 v[28:29], s[10:11], v132, s10, v[28:29]
	v_lshl_add_u64 v[34:35], v[28:29], 0, v[26:27]
	global_load_dwordx4 v[26:29], v[34:35], off offset:16 nt
	s_nop 0
	global_load_dwordx4 v[34:37], v[34:35], off nt

_Z12final_kernelPKDv4_fS1_PKfS3_Pf:
	s_load_dwordx4 s[4:7], s[0:1], 0x0
	s_load_dwordx2 s[2:3], s[0:1], 0x10
	s_load_dwordx2 s[8:9], s[0:1], 0x20
	v_and_b32_e32 v1, 0x1ff, v0
	v_readfirstlane_b32 s10, v0
	v_lshlrev_b32_e32 v2, 4, v1
	v_lshlrev_b32_e32 v3, 2, v1
	v_add_u32_e32 v4, 0x2000, v2
	v_add_u32_e32 v5, 0x4000, v2
	v_add_u32_e32 v6, 0x6000, v2
	v_add_u32_e32 v7, 0x8000, v2
	v_add_u32_e32 v8, 0xa000, v2
	v_add_u32_e32 v9, 0xc000, v2
	v_add_u32_e32 v10, 0xe000, v2
	s_cmpk_ge_u32 s10, 0x200
	s_waitcnt lgkmcnt(0)
	s_cselect_b32 s4, s6, s4
	s_cselect_b32 s5, s7, s5
	global_load_dwordx4 v[12:15], v2, s[4:5] nt
	global_load_dwordx4 v[16:19], v4, s[4:5] nt
	global_load_dwordx4 v[20:23], v5, s[4:5] nt
	global_load_dwordx4 v[24:27], v6, s[4:5] nt
	global_load_dwordx4 v[28:31], v7, s[4:5] nt
	global_load_dwordx4 v[32:35], v8, s[4:5] nt
	global_load_dwordx4 v[36:39], v9, s[4:5] nt
	global_load_dwordx4 v[40:43], v10, s[4:5] nt
	global_load_dword v44, v3, s[2:3] nt
	global_load_dword v45, v3, s[2:3] offset:2048 nt
	s_waitcnt vmcnt(2)
	v_max3_f32 v46, v12, v14, v16
	v_max3_f32 v47, v18, v20, v22
	v_max3_f32 v48, v24, v26, v28
	v_max3_f32 v49, v30, v32, v34
	v_max3_f32 v46, v46, v36, v38
	v_max3_f32 v47, v47, v40, v42
	v_max3_f32 v46, v46, v48, v49
	v_max_f32_e32 v46, v46, v47
	v_sub_f32_e32 v12, v12, v46
	v_sub_f32_e32 v14, v14, v46
	v_sub_f32_e32 v16, v16, v46
	v_sub_f32_e32 v18, v18, v46
	v_sub_f32_e32 v20, v20, v46
	v_sub_f32_e32 v22, v22, v46
	v_sub_f32_e32 v24, v24, v46
	v_sub_f32_e32 v26, v26, v46
	v_sub_f32_e32 v28, v28, v46
	v_sub_f32_e32 v30, v30, v46
	v_sub_f32_e32 v32, v32, v46
	v_sub_f32_e32 v34, v34, v46
	v_sub_f32_e32 v36, v36, v46
	v_sub_f32_e32 v38, v38, v46
	v_sub_f32_e32 v40, v40, v46
	v_sub_f32_e32 v42, v42, v46
	v_mul_f32_e32 v12, 0x3fb8aa3b, v12
	v_mul_f32_e32 v14, 0x3fb8aa3b, v14
	v_mul_f32_e32 v16, 0x3fb8aa3b, v16
	v_mul_f32_e32 v18, 0x3fb8aa3b, v18
	v_mul_f32_e32 v20, 0x3fb8aa3b, v20
	v_mul_f32_e32 v22, 0x3fb8aa3b, v22
	v_mul_f32_e32 v24, 0x3fb8aa3b, v24
	v_mul_f32_e32 v26, 0x3fb8aa3b, v26
	v_mul_f32_e32 v28, 0x3fb8aa3b, v28
	v_mul_f32_e32 v30, 0x3fb8aa3b, v30
	v_mul_f32_e32 v32, 0x3fb8aa3b, v32
	v_mul_f32_e32 v34, 0x3fb8aa3b, v34
	v_mul_f32_e32 v36, 0x3fb8aa3b, v36
	v_mul_f32_e32 v38, 0x3fb8aa3b, v38
	v_mul_f32_e32 v40, 0x3fb8aa3b, v40
	v_mul_f32_e32 v42, 0x3fb8aa3b, v42
	v_exp_f32_e32 v12, v12
	v_exp_f32_e32 v14, v14
	v_exp_f32_e32 v16, v16
	v_exp_f32_e32 v18, v18
	v_exp_f32_e32 v20, v20
	v_exp_f32_e32 v22, v22
	v_exp_f32_e32 v24, v24
	v_exp_f32_e32 v26, v26
	v_exp_f32_e32 v28, v28
	v_exp_f32_e32 v30, v30
	v_exp_f32_e32 v32, v32
	v_exp_f32_e32 v34, v34
	v_exp_f32_e32 v36, v36
	v_exp_f32_e32 v38, v38
	v_exp_f32_e32 v40, v40
	v_exp_f32_e32 v42, v42
	s_nop 0
	v_mul_f32_e32 v47, v13, v12
	v_mul_f32_e32 v48, v17, v16
	v_mul_f32_e32 v49, v21, v20
	v_mul_f32_e32 v50, v25, v24
	v_fmac_f32_e32 v47, v15, v14
	v_fmac_f32_e32 v48, v19, v18
	v_fmac_f32_e32 v49, v23, v22
	v_fmac_f32_e32 v50, v27, v26
	v_fmac_f32_e32 v47, v29, v28
	v_fmac_f32_e32 v48, v33, v32
	v_fmac_f32_e32 v49, v37, v36
	v_fmac_f32_e32 v50, v41, v40
	v_fmac_f32_e32 v47, v31, v30
	v_fmac_f32_e32 v48, v35, v34
	v_fmac_f32_e32 v49, v39, v38
	v_fmac_f32_e32 v50, v43, v42
	v_add_f32_e32 v47, v47, v48
	v_add_f32_e32 v49, v49, v50
	v_add_f32_e32 v47, v47, v49
	v_log_f32_e32 v47, v47
	s_mov_b32 s11, 0x3f317217
	v_mul_f32_e32 v48, 0x3f317217, v47
	v_fma_f32 v48, v47, s11, -v48
	v_fmamk_f32 v48, v47, 0x3377d1cf, v48
	v_fmac_f32_e32 v48, 0x3f317217, v47
	v_add_f32_e32 v46, v46, v48
	s_waitcnt vmcnt(0)
	v_sub_f32_e32 v46, v46, v44
	v_cmp_lt_f32_e32 vcc, 0, v45
	s_nop 1
	v_cndmask_b32_e32 v46, 0, v46, vcc
	v_cmp_lt_f32_e32 vcc, 0, v46
	v_max_f32_e32 v2, 0, v46
	s_nop 0
	v_cndmask_b32_e64 v3, 0, 1.0, vcc
	s_nop 0
	s_nop 0
	v_add_f32_dpp v2, v2, v2 quad_perm:[1,0,3,2] row_mask:0xf bank_mask:0xf
	v_add_f32_dpp v3, v3, v3 quad_perm:[1,0,3,2] row_mask:0xf bank_mask:0xf
	s_nop 0
	v_add_f32_dpp v2, v2, v2 quad_perm:[2,3,0,1] row_mask:0xf bank_mask:0xf
	v_add_f32_dpp v3, v3, v3 quad_perm:[2,3,0,1] row_mask:0xf bank_mask:0xf
	s_nop 0
	v_add_f32_dpp v2, v2, v2 row_half_mirror row_mask:0xf bank_mask:0xf
	v_add_f32_dpp v3, v3, v3 row_half_mirror row_mask:0xf bank_mask:0xf
	s_nop 0
	v_add_f32_dpp v2, v2, v2 row_mirror row_mask:0xf bank_mask:0xf
	v_add_f32_dpp v3, v3, v3 row_mirror row_mask:0xf bank_mask:0xf
	s_nop 0
	v_add_f32_dpp v2, v2, v2 row_bcast:15 row_mask:0xa bank_mask:0xf
	v_add_f32_dpp v3, v3, v3 row_bcast:15 row_mask:0xa bank_mask:0xf
	s_nop 0
	v_add_f32_dpp v2, v2, v2 row_bcast:31 row_mask:0xc bank_mask:0xf
	v_add_f32_dpp v3, v3, v3 row_bcast:31 row_mask:0xc bank_mask:0xf
	s_nop 1
	v_readlane_b32 s12, v2, 63
	v_readlane_b32 s13, v3, 63
	s_lshr_b32 s10, s10, 6
	s_lshl_b32 s10, s10, 2
	v_mov_b32_e32 v4, s10
	v_mov_b32_e32 v5, s12
	v_mov_b32_e32 v6, s13
	ds_write2_b32 v4, v5, v6 offset1:16
	s_waitcnt lgkmcnt(0)
	s_barrier
	s_cmp_lg_u32 s10, 0
	s_cbranch_scc1 .Lfin_end
	v_and_b32_e32 v4, 15, v0
	v_lshlrev_b32_e32 v4, 2, v4
	ds_read2_b32 v[2:3], v4 offset1:16
	s_waitcnt lgkmcnt(0)
	s_nop 0
	s_nop 0
	v_add_f32_dpp v2, v2, v2 quad_perm:[1,0,3,2] row_mask:0xf bank_mask:0xf
	v_add_f32_dpp v3, v3, v3 quad_perm:[1,0,3,2] row_mask:0xf bank_mask:0xf
	s_nop 0
	v_add_f32_dpp v2, v2, v2 quad_perm:[2,3,0,1] row_mask:0xf bank_mask:0xf
	v_add_f32_dpp v3, v3, v3 quad_perm:[2,3,0,1] row_mask:0xf bank_mask:0xf
	s_nop 0
	v_add_f32_dpp v2, v2, v2 row_half_mirror row_mask:0xf bank_mask:0xf
	v_add_f32_dpp v3, v3, v3 row_half_mirror row_mask:0xf bank_mask:0xf
	v_max_f32_e32 v5, 1.0, v3
	v_div_scale_f32 v6, s[12:13], v5, v5, v2
	v_rcp_f32_e32 v7, v6
	v_div_scale_f32 v8, vcc, v2, v5, v2
	v_fma_f32 v9, -v6, v7, 1.0
	v_fmac_f32_e32 v7, v9, v7
	v_mul_f32_e32 v9, v8, v7
	v_fma_f32 v10, -v6, v9, v8
	v_fmac_f32_e32 v9, v10, v7
	v_fma_f32 v6, -v6, v9, v8
	v_div_fmas_f32 v6, v6, v7, v9
	v_div_fixup_f32 v6, v6, v5, v2
	v_cmp_lt_f32_e32 vcc, 0, v3
	s_nop 1
	v_cndmask_b32_e32 v6, 0, v6, vcc
	s_nop 1
	v_add_f32_dpp v7, v6, v6 row_shl:8 row_mask:0xf bank_mask:0xf
	v_mov_b32_e32 v8, 0
	v_mul_f32_e32 v7, 0.5, v7
	v_cmp_eq_u32_e32 vcc, 0, v0
	s_and_saveexec_b64 s[12:13], vcc
	global_store_dword v8, v7, s[8:9]
